# v73 with default cache policy (no nt) on the rider's f32 weight loads
# baseline (speedup 1.0000x reference)
; DI void attn_unit_a8(unsigned char* lds, const AttnArgs& a) {
;     ...
;     auto w_issue = [&](int j) __attribute__((always_inline)) { const float* src; unsigned char* dst; int ld, n0, k0; bool gu; w_decode(j, src, dst, ld, n0, k0, gu);
;         const float* p = src + (size_t)(k0 + 4 * wid) * ld + n0 + wn4;
;         wq[0] = __builtin_nontemporal_load((const f32x4*)p); wq[1] = __builtin_nontemporal_load((const f32x4*)(p + ld));
;         wq[2] = __builtin_nontemporal_load((const f32x4*)(p + (size_t)2 * ld)); wq[3] = __builtin_nontemporal_load((const f32x4*)(p + (size_t)3 * ld)); };
; DI void attn_unit_d8(unsigned char* lds, const AttnArgs& a) {
;     ...
;     for (int t = a.t0; t < a.t1; t += 2) {
;         const int s1 = sb + 1 >= 5 ? sb - 4 : sb + 1, s2 = sb + 2 >= 5 ? sb - 3 : sb + 2, s3 = sb + 3 >= 5 ? sb - 2 : sb + 3, s4 = sb + 4 >= 5 ? sb - 1 : sb + 4;
;         { const int ta = t + 3, tb = t + 4; gload(ta < a.t1 ? ta : a.t1 - 1, kreg0, vreg0); gload(tb < a.t1 ? tb : a.t1 - 1, kreg1, vreg1); }
;         tile(lds + sb * D8_SLOT, lds + s1 * D8_SLOT, PaX, PbX, vX0, vX1, PaY, PbY, vY0, vY1);
;         tile(lds + s1 * D8_SLOT, lds + s2 * D8_SLOT, PaY, PbY, vY0, vY1, PaX, PbX, vX0, vX1);
;         lstore(s3, kreg0, vreg0); lstore(s4, kreg1, vreg1);
;         __syncthreads();
;         sb = s2;
;     }
;     o0[0] = mfma8(vY0, PaY, o0[0]); o1[0] = mfma8(vY0, PbY, o1[0]); o0[1] = mfma8(vY1, PaY, o0[1]); o1[1] = mfma8(vY1, PbY, o1[1]);
;     __builtin_amdgcn_s_setprio(0);
;     float lt0 = l0[0] + l0[1] + l0[2] + l0[3]; lt0 += __shfl_xor(lt0, 32);
;     float lt1 = l1[0] + l1[1] + l1[2] + l1[3]; lt1 += __shfl_xor(lt1, 32);
;     unsigned char* op = a.out8 + (size_t)(wid * 32 + r) * 1024 + 4 * h;
;     const float r0 = 16.0f / lt0, r1 = 16.0f * a.lam / lt1;
;     float ss = 0.f;
; #pragma unroll
;     for (int d = 0; d < 2; ++d)
; #pragma unroll
;         for (int i = 0; i < 16; ++i) { const float v = o0[d][i] * r0 - o1[d][i] * r1; o0[d][i] = v; ss += v * v; }
;     ss += __shfl_xor(ss, 32);
;     const float rinv = rsqrtf(ss * (1.0f / 64.0f) + EPS) * a.oscale * CAT_SCALE;
;     f32x4 ggv[2][4];
; #pragma unroll
;     for (int d = 0; d < 2; ++d)
; #pragma unroll
;         for (int g = 0; g < 4; ++g) ggv[d][g] = *(const f32x4*)(a.subg + 32 * d + 8 * g + 4 * h);
.Lmy_rd0_lgo:
	global_load_dwordx4 v[236:239], v235, s[84:85]
	s_add_u32 s84, s84, s80
	s_addc_u32 s85, s85, 0
	global_load_dwordx4 v[240:243], v235, s[84:85]
	s_add_u32 s84, s84, s80
	s_addc_u32 s85, s85, 0
	global_load_dwordx4 v[244:247], v235, s[84:85]
	s_add_u32 s84, s84, s80
	s_addc_u32 s85, s85, 0
	global_load_dwordx4 v[248:251], v235, s[84:85]
	s_mov_b32 s65, s58
	s_mov_b32 s58, s79
	s_mul_i32 s72, s80, 29
	s_add_u32 s84, s84, s72
	s_addc_u32 s85, s85, 0
	s_add_i32 s79, s79, 32
	v_xor_b32_e32 v252, 0x4000, v252
	v_xor_b32_e32 v253, 0x4000, v253
	s_add_i32 s61, s61, 1
	s_add_i32 s18, s46, 2
	s_cmpk_lt_u32 s46, 0x42
	s_mov_b32 s46, s18
	s_waitcnt vmcnt(6)
	ds_write_b64 v224, v[192:193]
	v_mfma_f32_32x32x64_f8f6f4 v[66:81], v[98:105], v[122:129], 0
	v_add_u32_e32 v98, 0x1400, v225
	v_add_u32_e32 v99, 0x1400, v107
	ds_write2_b32 v98, v202, v203 offset1:8
	s_waitcnt vmcnt(5)
	ds_write_b64 v106, v[194:195]
	ds_write2_b32 v99, v204, v205 offset1:8
	s_waitcnt lgkmcnt(0)
	s_barrier
	s_cbranch_scc1 .LBB0_663
	s_lshl_b64 s[14:15], s[14:15], 10
	s_add_u32 s6, s8, s14
	s_addc_u32 s15, s9, s15
	s_add_u32 s14, s6, s43
	v_mfma_f32_32x32x64_f8f6f4 v[50:65], v[154:161], v[138:145], v[50:65]
	s_addc_u32 s15, s15, 0
	v_mfma_f32_32x32x64_f8f6f4 v[2:17], v[154:161], v[130:137], v[2:17]
	v_mfma_f32_32x32x64_f8f6f4 v[34:49], v[146:153], v[138:145], v[34:49]
	v_mfma_f32_32x32x64_f8f6f4 v[18:33], v[146:153], v[130:137], v[18:33]
	s_setprio 0
	v_add_f32_e32 v66, v186, v187
	v_add_f32_e32 v66, v184, v66
	v_add_f32_e32 v66, v185, v66
	ds_bpermute_b32 v67, v1, v66
	v_add_f32_e32 v68, v190, v191
	v_add_f32_e32 v68, v188, v68
	v_add_f32_e32 v68, v189, v68
	ds_bpermute_b32 v69, v1, v68
	s_waitcnt lgkmcnt(1)
	v_add_f32_e32 v66, v66, v67
	v_div_scale_f32 v67, s[16:17], v66, v66, s36
	v_rcp_f32_e32 v70, v67
	s_waitcnt lgkmcnt(0)
	v_add_f32_e32 v68, v68, v69
	v_lshlrev_b32_e32 v178, 2, v214
	s_add_i32 s42, s42, s64
	v_fma_f32 v69, -v67, v70, 1.0
	v_fmac_f32_e32 v70, v69, v70
	v_div_scale_f32 v69, vcc, s36, v66, s36
	v_mul_f32_e32 v71, v69, v70
	v_fma_f32 v72, -v67, v71, v69
	v_fmac_f32_e32 v71, v72, v70
	v_fma_f32 v67, -v67, v71, v69
	v_div_scale_f32 v69, s[16:17], v68, v68, v211
	v_rcp_f32_e32 v72, v69
	v_div_fmas_f32 v67, v67, v70, v71
	v_div_fixup_f32 v66, v67, v66, s36
	s_cmpk_gt_i32 s42, 0x21f
	v_fma_f32 v67, -v69, v72, 1.0
	v_fmac_f32_e32 v72, v67, v72
	v_div_scale_f32 v67, vcc, v211, v68, v211
	v_mul_f32_e32 v70, v67, v72
	v_fma_f32 v71, -v69, v70, v67
	v_fmac_f32_e32 v70, v71, v72
	v_fma_f32 v67, -v69, v70, v67
	v_div_fmas_f32 v67, v67, v72, v70
	v_div_fixup_f32 v68, v67, v68, v211
	v_mul_f32_e32 v2, v2, v68
	v_fma_f32 v50, v50, v66, -v2
	v_mul_f32_e32 v2, v3, v68
	v_fma_f32 v51, v51, v66, -v2
	v_mul_f32_e32 v67, v51, v51
	v_mul_f32_e32 v2, v4, v68
	v_fmac_f32_e32 v67, v50, v50
	v_fma_f32 v52, v52, v66, -v2
	v_mul_f32_e32 v2, v5, v68
	v_fmac_f32_e32 v67, v52, v52
	v_fma_f32 v53, v53, v66, -v2
	v_mul_f32_e32 v2, v6, v68
	v_fmac_f32_e32 v67, v53, v53
	v_fma_f32 v54, v54, v66, -v2
	v_mul_f32_e32 v2, v7, v68
	v_fmac_f32_e32 v67, v54, v54
	v_fma_f32 v55, v55, v66, -v2
	v_mul_f32_e32 v2, v8, v68
	v_fmac_f32_e32 v67, v55, v55
	v_fma_f32 v56, v56, v66, -v2
	v_mul_f32_e32 v2, v9, v68
	v_fmac_f32_e32 v67, v56, v56
	v_fma_f32 v57, v57, v66, -v2
	v_mul_f32_e32 v2, v10, v68
	v_fmac_f32_e32 v67, v57, v57
	v_fma_f32 v58, v58, v66, -v2
	v_mul_f32_e32 v2, v11, v68
	v_fmac_f32_e32 v67, v58, v58
	v_fma_f32 v59, v59, v66, -v2
	v_mul_f32_e32 v2, v12, v68
	v_fmac_f32_e32 v67, v59, v59
	v_fma_f32 v60, v60, v66, -v2
	v_mul_f32_e32 v2, v13, v68
	v_fmac_f32_e32 v67, v60, v60
	v_fma_f32 v61, v61, v66, -v2
	v_mul_f32_e32 v14, v14, v68
	v_fmac_f32_e32 v67, v61, v61
	v_fma_f32 v62, v62, v66, -v14
	v_mul_f32_e32 v14, v15, v68
	v_fmac_f32_e32 v67, v62, v62
	v_fma_f32 v63, v63, v66, -v14
	v_mul_f32_e32 v14, v16, v68
	v_lshlrev_b32_e32 v69, 4, v214
	v_fmac_f32_e32 v67, v63, v63
	v_fma_f32 v64, v64, v66, -v14
	v_mul_f32_e32 v14, v17, v68
	global_load_dwordx4 v[2:5], v69, s[10:11] offset:224
	global_load_dwordx4 v[6:9], v69, s[10:11] offset:32
	global_load_dwordx4 v[10:13], v69, s[10:11]
	v_fmac_f32_e32 v67, v64, v64
	v_fma_f32 v65, v65, v66, -v14
	v_mul_f32_e32 v14, v18, v68
	v_fmac_f32_e32 v67, v65, v65
	v_fma_f32 v70, v34, v66, -v14
	v_mul_f32_e32 v14, v19, v68
	v_fmac_f32_e32 v67, v70, v70
	v_fma_f32 v71, v35, v66, -v14
	v_mul_f32_e32 v14, v20, v68
	v_fmac_f32_e32 v67, v71, v71
	v_fma_f32 v72, v36, v66, -v14
	v_mul_f32_e32 v14, v21, v68
	v_fmac_f32_e32 v67, v72, v72
	v_fma_f32 v73, v37, v66, -v14
	v_mul_f32_e32 v14, v22, v68
	v_fmac_f32_e32 v67, v73, v73
	v_fma_f32 v74, v38, v66, -v14
	v_mul_f32_e32 v14, v23, v68
	v_fmac_f32_e32 v67, v74, v74
	v_fma_f32 v75, v39, v66, -v14
	v_fmac_f32_e32 v67, v75, v75
	v_pk_mul_f32 v[14:15], v[24:25], v[68:69] op_sel_hi:[1,0]
	v_pk_mul_f32 v[22:23], v[32:33], v[68:69] op_sel_hi:[1,0]
	v_pk_fma_f32 v[34:35], v[40:41], v[66:67], v[14:15] op_sel_hi:[1,0,1] neg_lo:[0,0,1] neg_hi:[0,0,1]
	s_nop 0
	v_pk_mul_f32 v[14:15], v[34:35], v[34:35]
	s_nop 0
	v_add_f32_e32 v14, v14, v67
	v_add_f32_e32 v20, v15, v14
	v_pk_mul_f32 v[14:15], v[26:27], v[68:69] op_sel_hi:[1,0]
	s_nop 0
	v_pk_fma_f32 v[36:37], v[42:43], v[66:67], v[14:15] op_sel_hi:[1,0,1] neg_lo:[0,0,1] neg_hi:[0,0,1]
	global_load_dwordx4 v[14:17], v69, s[10:11] offset:64
	v_pk_mul_f32 v[18:19], v[36:37], v[36:37]
	v_pk_fma_f32 v[42:43], v[48:49], v[66:67], v[22:23] op_sel_hi:[1,0,1] neg_lo:[0,0,1] neg_hi:[0,0,1]
	v_add_f32_e32 v18, v18, v20
	v_add_f32_e32 v20, v19, v18
	v_pk_mul_f32 v[18:19], v[28:29], v[68:69] op_sel_hi:[1,0]
	v_pk_mul_f32 v[22:23], v[42:43], v[42:43]
	v_pk_fma_f32 v[38:39], v[44:45], v[66:67], v[18:19] op_sel_hi:[1,0,1] neg_lo:[0,0,1] neg_hi:[0,0,1]
	s_nop 0
	v_pk_mul_f32 v[18:19], v[38:39], v[38:39]
	s_nop 0
	v_add_f32_e32 v18, v18, v20
	v_add_f32_e32 v20, v19, v18
	v_pk_mul_f32 v[18:19], v[30:31], v[68:69] op_sel_hi:[1,0]
	s_nop 0
	v_pk_fma_f32 v[40:41], v[46:47], v[66:67], v[18:19] op_sel_hi:[1,0,1] neg_lo:[0,0,1] neg_hi:[0,0,1]
	s_nop 0
	v_pk_mul_f32 v[18:19], v[40:41], v[40:41]
	s_nop 0
	v_add_f32_e32 v18, v18, v20
	v_add_f32_e32 v24, v19, v18
	v_add_f32_e32 v22, v22, v24
	v_add_f32_e32 v26, v23, v22
	ds_bpermute_b32 v27, v1, v26
	global_load_dwordx4 v[18:21], v69, s[10:11] offset:96
	global_load_dwordx4 v[22:25], v69, s[10:11] offset:192
	s_waitcnt lgkmcnt(0)
; DI unsigned pk4_fp8(float a, float b, float c, float d) { int r = 0; r = __builtin_amdgcn_cvt_pk_fp8_f32(a, b, r, false); r = __builtin_amdgcn_cvt_pk_fp8_f32(c, d, r, true); return (unsigned)r; }
; DI float clamp448(float x) { return __builtin_amdgcn_fmed3f(x, -448.0f, 448.0f); }
; DI void attn_unit_d8(unsigned char* lds, const AttnArgs& a) {
;     ...
;     const float r0 = 16.0f / lt0, r1 = 16.0f * a.lam / lt1;
;     float ss = 0.f;
; #pragma unroll
;     for (int d = 0; d < 2; ++d)
; #pragma unroll
;         for (int i = 0; i < 16; ++i) { const float v = o0[d][i] * r0 - o1[d][i] * r1; o0[d][i] = v; ss += v * v; }
;     ss += __shfl_xor(ss, 32);
;     const float rinv = rsqrtf(ss * (1.0f / 64.0f) + EPS) * a.oscale * CAT_SCALE;
;     f32x4 ggv[2][4];
; #pragma unroll
;     for (int d = 0; d < 2; ++d)
; #pragma unroll
;         for (int g = 0; g < 4; ++g) ggv[d][g] = *(const f32x4*)(a.subg + 32 * d + 8 * g + 4 * h);
;     asm volatile("" : "+v"(ggv[0][0]), "+v"(ggv[1][3]));
; #pragma unroll
;     for (int d = 0; d < 2; ++d)
; #pragma unroll
;         for (int g = 0; g < 4; ++g) { const f32x4 gg = ggv[d][g];
;             *(unsigned*)(op + 32 * d + 8 * g) = pk4_fp8(clamp448(o0[d][4 * g] * rinv * gg[0]), clamp448(o0[d][4 * g + 1] * rinv * gg[1]), clamp448(o0[d][4 * g + 2] * rinv * gg[2]), clamp448(o0[d][4 * g + 3] * rinv * gg[3])); }
	v_add_f32_e32 v26, v26, v27
	v_fmamk_f32 v26, v26, 0x3c800000, v212
	v_mul_f32_e32 v27, 0x4b800000, v26
	v_cmp_gt_f32_e32 vcc, s39, v26
	s_nop 1
	v_cndmask_b32_e32 v30, v26, v27, vcc
	global_load_dwordx4 v[26:29], v69, s[10:11] offset:128
	v_rsq_f32_e32 v32, v30
	v_lshlrev_b64 v[30:31], 10, v[180:181]
	v_lshl_add_u64 v[44:45], s[14:15], 0, v[30:31]
	v_lshl_add_u64 v[44:45], v[44:45], 0, v[178:179]
	v_mul_f32_e32 v30, 0x45800000, v32
	v_cndmask_b32_e32 v30, v32, v30, vcc
	v_mul_f32_e32 v48, 0x3f4ccccd, v30
	global_load_dwordx4 v[30:33], v69, s[10:11] offset:160
	v_mul_f32_e32 v48, 0x41800000, v48
	s_waitcnt vmcnt(5)
	v_mul_f32_e32 v49, v50, v48
	v_mul_f32_e32 v10, v10, v49
	v_mul_f32_e32 v49, v51, v48
	v_mul_f32_e32 v11, v11, v49
	v_mul_f32_e32 v49, v52, v48
	v_med3_f32 v10, v10, s40, v213
	v_med3_f32 v11, v11, s40, v213
	v_mul_f32_e32 v12, v12, v49
	s_nop 0
	v_cvt_pk_fp8_f32 v49, v10, v11
	v_mul_f32_e32 v10, v53, v48
	v_mul_f32_e32 v10, v13, v10
	v_med3_f32 v12, v12, s40, v213
	v_med3_f32 v10, v10, s40, v213
	v_cvt_pk_fp8_f32 v49, v12, v10 op_sel:[0,0,1]
	v_mul_f32_e32 v10, v54, v48
	v_mul_f32_e32 v6, v6, v10
	v_mul_f32_e32 v10, v55, v48
	v_mul_f32_e32 v7, v7, v10
	v_mul_f32_e32 v10, v56, v48
	v_med3_f32 v6, v6, s40, v213
	v_med3_f32 v7, v7, s40, v213
	v_mul_f32_e32 v8, v8, v10
	s_nop 0
	v_cvt_pk_fp8_f32 v10, v6, v7
	v_mul_f32_e32 v6, v57, v48
	v_mul_f32_e32 v6, v9, v6
	v_med3_f32 v8, v8, s40, v213
	v_med3_f32 v6, v6, s40, v213
	v_cvt_pk_fp8_f32 v10, v8, v6 op_sel:[0,0,1]
	v_add_co_u32_e32 v6, vcc, s41, v44
	v_lshl_add_u64 v[46:47], v[44:45], 0, s[12:13]
	s_nop 0
	v_addc_co_u32_e32 v7, vcc, 0, v45, vcc
	global_store_dword v[6:7], v49, off offset:768
	global_store_dword v[46:47], v10, off offset:8
	v_mul_f32_e32 v6, v58, v48
	v_mul_f32_e32 v7, v59, v48
	s_waitcnt vmcnt(6)
	v_mul_f32_e32 v6, v14, v6
	v_mul_f32_e32 v7, v15, v7
	v_med3_f32 v6, v6, s40, v213
	v_med3_f32 v7, v7, s40, v213
	s_nop 0
	v_cvt_pk_fp8_f32 v9, v6, v7
	v_mul_f32_e32 v8, v60, v48
	v_mul_f32_e32 v6, v61, v48
	v_mul_f32_e32 v8, v16, v8
	v_mul_f32_e32 v6, v17, v6
	v_med3_f32 v8, v8, s40, v213
	v_med3_f32 v6, v6, s40, v213
	v_cvt_pk_fp8_f32 v9, v8, v6 op_sel:[0,0,1]
	v_mul_f32_e32 v6, v62, v48
	v_mul_f32_e32 v7, v63, v48
	s_nop 0
	v_mul_f32_e32 v8, v64, v48
	s_nop 0
	s_waitcnt vmcnt(5)
	v_mul_f32_e32 v6, v18, v6
	v_mul_f32_e32 v7, v19, v7
	v_med3_f32 v6, v6, s40, v213
	v_med3_f32 v7, v7, s40, v213
	v_cvt_pk_fp8_f32 v10, v6, v7
	v_mul_f32_e32 v6, v65, v48
	v_mul_f32_e32 v8, v20, v8
	v_mul_f32_e32 v6, v21, v6
	v_med3_f32 v8, v8, s40, v213
	v_med3_f32 v6, v6, s40, v213
	v_cvt_pk_fp8_f32 v10, v8, v6 op_sel:[0,0,1]
	v_mul_f32_e32 v6, v70, v48
	v_mul_f32_e32 v7, v71, v48
	s_waitcnt vmcnt(3)
	v_mul_f32_e32 v6, v26, v6
	v_mul_f32_e32 v7, v27, v7
	v_med3_f32 v6, v6, s40, v213
	v_med3_f32 v7, v7, s40, v213
	v_cvt_pk_fp8_f32 v11, v6, v7
	v_mul_f32_e32 v8, v72, v48
	v_mul_f32_e32 v6, v73, v48
	v_mul_f32_e32 v8, v28, v8
	v_mul_f32_e32 v6, v29, v6
	v_med3_f32 v8, v8, s40, v213
	v_med3_f32 v6, v6, s40, v213
	v_cvt_pk_fp8_f32 v11, v8, v6 op_sel:[0,0,1]
	v_mul_f32_e32 v6, v74, v48
	v_mul_f32_e32 v7, v75, v48
	s_waitcnt vmcnt(2)
	v_mul_f32_e32 v6, v30, v6
	v_mul_f32_e32 v7, v31, v7
	v_med3_f32 v6, v6, s40, v213
	v_med3_f32 v7, v7, s40, v213
	s_nop 0
	v_cvt_pk_fp8_f32 v12, v6, v7
	v_mul_f32_e32 v8, v34, v48
	v_mul_f32_e32 v6, v35, v48
	v_mul_f32_e32 v8, v32, v8
	v_mul_f32_e32 v6, v33, v6
	v_med3_f32 v8, v8, s40, v213
	v_med3_f32 v6, v6, s40, v213
	v_cvt_pk_fp8_f32 v12, v8, v6 op_sel:[0,0,1]
	v_mul_f32_e32 v6, v36, v48
	v_mul_f32_e32 v7, v37, v48
	v_mul_f32_e32 v6, v22, v6
	v_mul_f32_e32 v7, v23, v7
	global_store_dword v[46:47], v9, off offset:16
	global_store_dword v[46:47], v10, off offset:24
	global_store_dword v[46:47], v11, off offset:32
	global_store_dword v[46:47], v12, off offset:40
	v_med3_f32 v6, v6, s40, v213
	v_med3_f32 v7, v7, s40, v213
	s_nop 0
	v_cvt_pk_fp8_f32 v9, v6, v7
	v_mul_f32_e32 v8, v38, v48
	v_mul_f32_e32 v6, v39, v48
	v_mul_f32_e32 v8, v24, v8
	v_mul_f32_e32 v6, v25, v6
	v_med3_f32 v8, v8, s40, v213
	v_med3_f32 v6, v6, s40, v213
	v_cvt_pk_fp8_f32 v9, v8, v6 op_sel:[0,0,1]
	v_mul_f32_e32 v6, v40, v48
	v_mul_f32_e32 v2, v2, v6
	v_mul_f32_e32 v6, v41, v48
	v_mul_f32_e32 v3, v3, v6
	v_mul_f32_e32 v6, v42, v48
	v_med3_f32 v2, v2, s40, v213
	v_med3_f32 v3, v3, s40, v213
	v_mul_f32_e32 v4, v4, v6
	s_nop 0
	v_cvt_pk_fp8_f32 v6, v2, v3
	v_mul_f32_e32 v2, v43, v48
	v_mul_f32_e32 v2, v5, v2
	v_med3_f32 v4, v4, s40, v213
	v_med3_f32 v2, v2, s40, v213
	v_cvt_pk_fp8_f32 v6, v4, v2 op_sel:[0,0,1]
	global_store_dword v[46:47], v9, off offset:48
	global_store_dword v[46:47], v6, off offset:56
	s_cbranch_scc0 .LBB0_656

; DI unsigned pk4_fp8(float a, float b, float c, float d) { int r = 0; r = __builtin_amdgcn_cvt_pk_fp8_f32(a, b, r, false); r = __builtin_amdgcn_cvt_pk_fp8_f32(c, d, r, true); return (unsigned)r; }
; DI float clamp448(float x) { return __builtin_amdgcn_fmed3f(x, -448.0f, 448.0f); }
; DI void attn_unit_a8(unsigned char* lds, const AttnArgs& a) {
;     ...
;     auto w_issue = [&](int j) __attribute__((always_inline)) { const float* src; unsigned char* dst; int ld, n0, k0; bool gu; w_decode(j, src, dst, ld, n0, k0, gu);
;         const float* p = src + (size_t)(k0 + 4 * wid) * ld + n0 + wn4;
;         wq[0] = __builtin_nontemporal_load((const f32x4*)p); wq[1] = __builtin_nontemporal_load((const f32x4*)(p + ld));
;         wq[2] = __builtin_nontemporal_load((const f32x4*)(p + (size_t)2 * ld)); wq[3] = __builtin_nontemporal_load((const f32x4*)(p + (size_t)3 * ld)); };
; DI void attn_unit_d8(unsigned char* lds, const AttnArgs& a) {
;     ...
;     float lt0 = l0[0] + l0[1] + l0[2] + l0[3]; lt0 += __shfl_xor(lt0, 32);
;     float lt1 = l1[0] + l1[1] + l1[2] + l1[3]; lt1 += __shfl_xor(lt1, 32);
;     unsigned char* op = a.out8 + (size_t)(wid * 32 + r) * 1024 + 4 * h;
;     const float r0 = 16.0f / lt0, r1 = 16.0f * a.lam / lt1;
;     float ss = 0.f;
; #pragma unroll
;     for (int d = 0; d < 2; ++d)
; #pragma unroll
;         for (int i = 0; i < 16; ++i) { const float v = o0[d][i] * r0 - o1[d][i] * r1; o0[d][i] = v; ss += v * v; }
;     ss += __shfl_xor(ss, 32);
;     const float rinv = rsqrtf(ss * (1.0f / 64.0f) + EPS) * a.oscale * CAT_SCALE;
;     f32x4 ggv[2][4];
; #pragma unroll
;     for (int d = 0; d < 2; ++d)
; #pragma unroll
;         for (int g = 0; g < 4; ++g) ggv[d][g] = *(const f32x4*)(a.subg + 32 * d + 8 * g + 4 * h);
;     asm volatile("" : "+v"(ggv[0][0]), "+v"(ggv[1][3]));
; #pragma unroll
;     for (int d = 0; d < 2; ++d)
; #pragma unroll
;         for (int g = 0; g < 4; ++g) { const f32x4 gg = ggv[d][g];
;             *(unsigned*)(op + 32 * d + 8 * g) = pk4_fp8(clamp448(o0[d][4 * g] * rinv * gg[0]), clamp448(o0[d][4 * g + 1] * rinv * gg[1]), clamp448(o0[d][4 * g + 2] * rinv * gg[2]), clamp448(o0[d][4 * g + 3] * rinv * gg[3])); }
.Lmy_rd1_lgo:
	global_load_dwordx4 v[236:239], v235, s[84:85]
	s_add_u32 s84, s84, s80
	s_addc_u32 s85, s85, 0
	global_load_dwordx4 v[240:243], v235, s[84:85]
	s_add_u32 s84, s84, s80
	s_addc_u32 s85, s85, 0
	global_load_dwordx4 v[244:247], v235, s[84:85]
	s_add_u32 s84, s84, s80
	s_addc_u32 s85, s85, 0
	global_load_dwordx4 v[248:251], v235, s[84:85]
	s_mov_b32 s65, s64
	s_mov_b32 s64, s79
	s_mul_i32 s72, s80, 29
	s_add_u32 s84, s84, s72
	s_addc_u32 s85, s85, 0
	s_add_i32 s79, s79, 32
	v_xor_b32_e32 v252, 0x4000, v252
	v_xor_b32_e32 v253, 0x4000, v253
	s_add_i32 s61, s61, 1
	s_cmpk_lt_u32 s22, 0x42
	s_waitcnt vmcnt(6)
	ds_write_b64 v224, v[194:195]
	v_mfma_f32_32x32x64_f8f6f4 v[66:81], v[98:105], v[122:129], 0
	v_add_u32_e32 v98, s51, v218
	v_add_u32_e32 v99, 0x1400, v106
	v_add_u32_e32 v98, 0x1400, v98
	ds_write2_b32 v99, v204, v205 offset1:8
	s_waitcnt vmcnt(5)
	ds_write_b64 v107, v[196:197]
	ds_write2_b32 v98, v206, v207 offset1:8
	s_waitcnt lgkmcnt(0)
	s_barrier
	s_cbranch_scc1 .LBB0_1888
	s_lshl_b64 s[16:17], s[16:17], 10
	s_add_u32 s8, s10, s16
	s_addc_u32 s17, s11, s17
	s_add_u32 s16, s8, s47
	v_mfma_f32_32x32x64_f8f6f4 v[50:65], v[154:161], v[138:145], v[50:65]
	s_addc_u32 s17, s17, 0
	v_mfma_f32_32x32x64_f8f6f4 v[2:17], v[154:161], v[130:137], v[2:17]
	v_mfma_f32_32x32x64_f8f6f4 v[34:49], v[146:153], v[138:145], v[34:49]
	v_mfma_f32_32x32x64_f8f6f4 v[18:33], v[146:153], v[130:137], v[18:33]
	s_setprio 0
	v_add_f32_e32 v66, v188, v189
	v_add_f32_e32 v66, v186, v66
	v_add_f32_e32 v66, v187, v66
	ds_bpermute_b32 v67, v1, v66
	v_add_f32_e32 v68, v192, v193
	v_add_f32_e32 v68, v190, v68
	v_add_f32_e32 v68, v191, v68
	ds_bpermute_b32 v69, v1, v68
	s_waitcnt lgkmcnt(1)
	v_add_f32_e32 v66, v66, v67
	v_div_scale_f32 v67, s[18:19], v66, v66, s36
	v_rcp_f32_e32 v70, v67
	s_waitcnt lgkmcnt(0)
	v_add_f32_e32 v68, v68, v69
	v_lshlrev_b32_e32 v178, 2, v217
	s_add_i32 s46, s46, s60
	v_fma_f32 v69, -v67, v70, 1.0
	v_fmac_f32_e32 v70, v69, v70
	v_div_scale_f32 v69, vcc, s36, v66, s36
	v_mul_f32_e32 v71, v69, v70
	v_fma_f32 v72, -v67, v71, v69
	v_fmac_f32_e32 v71, v72, v70
	v_fma_f32 v67, -v67, v71, v69
	v_div_scale_f32 v69, s[18:19], v68, v68, v214
	v_rcp_f32_e32 v72, v69
	v_div_fmas_f32 v67, v67, v70, v71
	v_div_fixup_f32 v66, v67, v66, s36
	s_cmpk_gt_i32 s46, 0x1ff
	v_fma_f32 v67, -v69, v72, 1.0
	v_fmac_f32_e32 v72, v67, v72
	v_div_scale_f32 v67, vcc, v214, v68, v214
	v_mul_f32_e32 v70, v67, v72
	v_fma_f32 v71, -v69, v70, v67
	v_fmac_f32_e32 v70, v71, v72
	v_fma_f32 v67, -v69, v70, v67
	v_div_fmas_f32 v67, v67, v72, v70
	v_div_fixup_f32 v68, v67, v68, v214
	v_mul_f32_e32 v2, v2, v68
	v_fma_f32 v50, v50, v66, -v2
	v_mul_f32_e32 v2, v3, v68
	v_fma_f32 v51, v51, v66, -v2
	v_mul_f32_e32 v67, v51, v51
	v_mul_f32_e32 v2, v4, v68
	v_fmac_f32_e32 v67, v50, v50
	v_fma_f32 v52, v52, v66, -v2
	v_mul_f32_e32 v2, v5, v68
	v_fmac_f32_e32 v67, v52, v52
	v_fma_f32 v53, v53, v66, -v2
	v_mul_f32_e32 v2, v6, v68
	v_fmac_f32_e32 v67, v53, v53
	v_fma_f32 v54, v54, v66, -v2
	v_mul_f32_e32 v2, v7, v68
	v_fmac_f32_e32 v67, v54, v54
	v_fma_f32 v55, v55, v66, -v2
	v_mul_f32_e32 v2, v8, v68
	v_fmac_f32_e32 v67, v55, v55
	v_fma_f32 v56, v56, v66, -v2
	v_mul_f32_e32 v2, v9, v68
	v_fmac_f32_e32 v67, v56, v56
	v_fma_f32 v57, v57, v66, -v2
	v_mul_f32_e32 v2, v10, v68
	v_fmac_f32_e32 v67, v57, v57
	v_fma_f32 v58, v58, v66, -v2
	v_mul_f32_e32 v2, v11, v68
	v_fmac_f32_e32 v67, v58, v58
	v_fma_f32 v59, v59, v66, -v2
	v_mul_f32_e32 v2, v12, v68
	v_fmac_f32_e32 v67, v59, v59
	v_fma_f32 v60, v60, v66, -v2
	v_mul_f32_e32 v2, v13, v68
	v_fmac_f32_e32 v67, v60, v60
	v_fma_f32 v61, v61, v66, -v2
	v_mul_f32_e32 v14, v14, v68
	v_fmac_f32_e32 v67, v61, v61
	v_fma_f32 v62, v62, v66, -v14
	v_mul_f32_e32 v14, v15, v68
	v_fmac_f32_e32 v67, v62, v62
	v_fma_f32 v63, v63, v66, -v14
	v_mul_f32_e32 v14, v16, v68
	v_lshlrev_b32_e32 v69, 4, v217
	v_fmac_f32_e32 v67, v63, v63
	v_fma_f32 v64, v64, v66, -v14
	v_mul_f32_e32 v14, v17, v68
	global_load_dwordx4 v[2:5], v69, s[12:13] offset:480
	global_load_dwordx4 v[6:9], v69, s[12:13] offset:288
	global_load_dwordx4 v[10:13], v69, s[12:13] offset:256
	v_fmac_f32_e32 v67, v64, v64
	v_fma_f32 v65, v65, v66, -v14
	v_mul_f32_e32 v14, v18, v68
	v_fmac_f32_e32 v67, v65, v65
	v_fma_f32 v70, v34, v66, -v14
	v_mul_f32_e32 v14, v19, v68
	v_fmac_f32_e32 v67, v70, v70
	v_fma_f32 v71, v35, v66, -v14
	v_mul_f32_e32 v14, v20, v68
	v_fmac_f32_e32 v67, v71, v71
	v_fma_f32 v72, v36, v66, -v14
	v_mul_f32_e32 v14, v21, v68
	v_fmac_f32_e32 v67, v72, v72
	v_fma_f32 v73, v37, v66, -v14
	v_mul_f32_e32 v14, v22, v68
	v_fmac_f32_e32 v67, v73, v73
	v_fma_f32 v74, v38, v66, -v14
	v_mul_f32_e32 v14, v23, v68
	v_fmac_f32_e32 v67, v74, v74
	v_fma_f32 v75, v39, v66, -v14
	v_fmac_f32_e32 v67, v75, v75
	v_pk_mul_f32 v[14:15], v[24:25], v[68:69] op_sel_hi:[1,0]
	v_pk_mul_f32 v[22:23], v[32:33], v[68:69] op_sel_hi:[1,0]
	v_pk_fma_f32 v[34:35], v[40:41], v[66:67], v[14:15] op_sel_hi:[1,0,1] neg_lo:[0,0,1] neg_hi:[0,0,1]
	s_nop 0
	v_pk_mul_f32 v[14:15], v[34:35], v[34:35]
	s_nop 0
	v_add_f32_e32 v14, v14, v67
	v_add_f32_e32 v20, v15, v14
	v_pk_mul_f32 v[14:15], v[26:27], v[68:69] op_sel_hi:[1,0]
	s_nop 0
	v_pk_fma_f32 v[36:37], v[42:43], v[66:67], v[14:15] op_sel_hi:[1,0,1] neg_lo:[0,0,1] neg_hi:[0,0,1]
	global_load_dwordx4 v[14:17], v69, s[12:13] offset:320
	v_pk_mul_f32 v[18:19], v[36:37], v[36:37]
	v_pk_fma_f32 v[42:43], v[48:49], v[66:67], v[22:23] op_sel_hi:[1,0,1] neg_lo:[0,0,1] neg_hi:[0,0,1]
	v_add_f32_e32 v18, v18, v20
	v_add_f32_e32 v20, v19, v18
	v_pk_mul_f32 v[18:19], v[28:29], v[68:69] op_sel_hi:[1,0]
	v_pk_mul_f32 v[22:23], v[42:43], v[42:43]
	v_pk_fma_f32 v[38:39], v[44:45], v[66:67], v[18:19] op_sel_hi:[1,0,1] neg_lo:[0,0,1] neg_hi:[0,0,1]
	s_nop 0
	v_pk_mul_f32 v[18:19], v[38:39], v[38:39]
	s_nop 0
	v_add_f32_e32 v18, v18, v20
	v_add_f32_e32 v20, v19, v18
	v_pk_mul_f32 v[18:19], v[30:31], v[68:69] op_sel_hi:[1,0]
	s_nop 0
	v_pk_fma_f32 v[40:41], v[46:47], v[66:67], v[18:19] op_sel_hi:[1,0,1] neg_lo:[0,0,1] neg_hi:[0,0,1]
	s_nop 0
	v_pk_mul_f32 v[18:19], v[40:41], v[40:41]
	s_nop 0
	v_add_f32_e32 v18, v18, v20
	v_add_f32_e32 v24, v19, v18
	v_add_f32_e32 v22, v22, v24
	v_add_f32_e32 v26, v23, v22
	ds_bpermute_b32 v27, v1, v26
	global_load_dwordx4 v[18:21], v69, s[12:13] offset:352
	global_load_dwordx4 v[22:25], v69, s[12:13] offset:448
	s_waitcnt lgkmcnt(0)
; DI unsigned pk4_fp8(float a, float b, float c, float d) { int r = 0; r = __builtin_amdgcn_cvt_pk_fp8_f32(a, b, r, false); r = __builtin_amdgcn_cvt_pk_fp8_f32(c, d, r, true); return (unsigned)r; }
; DI float clamp448(float x) { return __builtin_amdgcn_fmed3f(x, -448.0f, 448.0f); }
; DI void attn_unit_d8(unsigned char* lds, const AttnArgs& a) {
;     ...
;     ss += __shfl_xor(ss, 32);
;     const float rinv = rsqrtf(ss * (1.0f / 64.0f) + EPS) * a.oscale * CAT_SCALE;
;     f32x4 ggv[2][4];
; #pragma unroll
;     for (int d = 0; d < 2; ++d)
; #pragma unroll
;         for (int g = 0; g < 4; ++g) ggv[d][g] = *(const f32x4*)(a.subg + 32 * d + 8 * g + 4 * h);
;     asm volatile("" : "+v"(ggv[0][0]), "+v"(ggv[1][3]));
; #pragma unroll
;     for (int d = 0; d < 2; ++d)
; #pragma unroll
;         for (int g = 0; g < 4; ++g) { const f32x4 gg = ggv[d][g];
;             *(unsigned*)(op + 32 * d + 8 * g) = pk4_fp8(clamp448(o0[d][4 * g] * rinv * gg[0]), clamp448(o0[d][4 * g + 1] * rinv * gg[1]), clamp448(o0[d][4 * g + 2] * rinv * gg[2]), clamp448(o0[d][4 * g + 3] * rinv * gg[3])); }
	v_add_f32_e32 v26, v26, v27
	v_fmamk_f32 v26, v26, 0x3c800000, v215
	v_mul_f32_e32 v27, 0x4b800000, v26
	v_cmp_gt_f32_e32 vcc, s41, v26
	s_nop 1
	v_cndmask_b32_e32 v30, v26, v27, vcc
	global_load_dwordx4 v[26:29], v69, s[12:13] offset:384
	v_rsq_f32_e32 v32, v30
	v_lshlrev_b64 v[30:31], 10, v[180:181]
	v_lshl_add_u64 v[44:45], s[16:17], 0, v[30:31]
	v_lshl_add_u64 v[44:45], v[44:45], 0, v[178:179]
	v_mul_f32_e32 v30, 0x45800000, v32
	v_cndmask_b32_e32 v30, v32, v30, vcc
	v_mul_f32_e32 v48, v213, v30
	global_load_dwordx4 v[30:33], v69, s[12:13] offset:416
	v_mul_f32_e32 v48, 0x41800000, v48
	s_waitcnt vmcnt(5)
	v_mul_f32_e32 v49, v50, v48
	v_mul_f32_e32 v10, v10, v49
	v_mul_f32_e32 v49, v51, v48
	v_mul_f32_e32 v11, v11, v49
	v_mul_f32_e32 v49, v52, v48
	v_med3_f32 v10, v10, s42, v216
	v_med3_f32 v11, v11, s42, v216
	v_mul_f32_e32 v12, v12, v49
	s_nop 0
	v_cvt_pk_fp8_f32 v49, v10, v11
	v_mul_f32_e32 v10, v53, v48
	v_mul_f32_e32 v10, v13, v10
	v_med3_f32 v12, v12, s42, v216
	v_med3_f32 v10, v10, s42, v216
	v_cvt_pk_fp8_f32 v49, v12, v10 op_sel:[0,0,1]
	v_mul_f32_e32 v10, v54, v48
	v_mul_f32_e32 v6, v6, v10
	v_mul_f32_e32 v10, v55, v48
	v_mul_f32_e32 v7, v7, v10
	v_mul_f32_e32 v10, v56, v48
	v_med3_f32 v6, v6, s42, v216
	v_med3_f32 v7, v7, s42, v216
	v_mul_f32_e32 v8, v8, v10
	s_nop 0
	v_cvt_pk_fp8_f32 v10, v6, v7
	v_mul_f32_e32 v6, v57, v48
	v_mul_f32_e32 v6, v9, v6
	v_med3_f32 v8, v8, s42, v216
	v_med3_f32 v6, v6, s42, v216
	v_cvt_pk_fp8_f32 v10, v8, v6 op_sel:[0,0,1]
	v_add_co_u32_e32 v6, vcc, s43, v44
	v_lshl_add_u64 v[46:47], v[44:45], 0, s[14:15]
	s_nop 0
	v_addc_co_u32_e32 v7, vcc, 0, v45, vcc
	global_store_dword v[6:7], v49, off offset:768
	global_store_dword v[46:47], v10, off offset:8
	v_mul_f32_e32 v6, v58, v48
	v_mul_f32_e32 v7, v59, v48
	s_waitcnt vmcnt(6)
	v_mul_f32_e32 v6, v14, v6
	v_mul_f32_e32 v7, v15, v7
	v_med3_f32 v6, v6, s42, v216
	v_med3_f32 v7, v7, s42, v216
	s_nop 0
	v_cvt_pk_fp8_f32 v9, v6, v7
	v_mul_f32_e32 v8, v60, v48
	v_mul_f32_e32 v6, v61, v48
	v_mul_f32_e32 v8, v16, v8
	v_mul_f32_e32 v6, v17, v6
	v_med3_f32 v8, v8, s42, v216
	v_med3_f32 v6, v6, s42, v216
	v_cvt_pk_fp8_f32 v9, v8, v6 op_sel:[0,0,1]
	v_mul_f32_e32 v6, v62, v48
	v_mul_f32_e32 v7, v63, v48
	s_nop 0
	v_mul_f32_e32 v8, v64, v48
	s_nop 0
	s_waitcnt vmcnt(5)
	v_mul_f32_e32 v6, v18, v6
	v_mul_f32_e32 v7, v19, v7
	v_med3_f32 v6, v6, s42, v216
	v_med3_f32 v7, v7, s42, v216
	v_cvt_pk_fp8_f32 v10, v6, v7
	v_mul_f32_e32 v6, v65, v48
	v_mul_f32_e32 v8, v20, v8
	v_mul_f32_e32 v6, v21, v6
	v_med3_f32 v8, v8, s42, v216
	v_med3_f32 v6, v6, s42, v216
	v_cvt_pk_fp8_f32 v10, v8, v6 op_sel:[0,0,1]
	v_mul_f32_e32 v6, v70, v48
	v_mul_f32_e32 v7, v71, v48
	s_waitcnt vmcnt(3)
	v_mul_f32_e32 v6, v26, v6
	v_mul_f32_e32 v7, v27, v7
	v_med3_f32 v6, v6, s42, v216
	v_med3_f32 v7, v7, s42, v216
	v_cvt_pk_fp8_f32 v11, v6, v7
	v_mul_f32_e32 v8, v72, v48
	v_mul_f32_e32 v6, v73, v48
	v_mul_f32_e32 v8, v28, v8
	v_mul_f32_e32 v6, v29, v6
	v_med3_f32 v8, v8, s42, v216
	v_med3_f32 v6, v6, s42, v216
	v_cvt_pk_fp8_f32 v11, v8, v6 op_sel:[0,0,1]
	v_mul_f32_e32 v6, v74, v48
	v_mul_f32_e32 v7, v75, v48
	s_waitcnt vmcnt(2)
	v_mul_f32_e32 v6, v30, v6
	v_mul_f32_e32 v7, v31, v7
	v_med3_f32 v6, v6, s42, v216
	v_med3_f32 v7, v7, s42, v216
	s_nop 0
	v_cvt_pk_fp8_f32 v12, v6, v7
	v_mul_f32_e32 v8, v34, v48
	v_mul_f32_e32 v6, v35, v48
	v_mul_f32_e32 v8, v32, v8
	v_mul_f32_e32 v6, v33, v6
	v_med3_f32 v8, v8, s42, v216
	v_med3_f32 v6, v6, s42, v216
	v_cvt_pk_fp8_f32 v12, v8, v6 op_sel:[0,0,1]
	v_mul_f32_e32 v6, v36, v48
	v_mul_f32_e32 v7, v37, v48
	v_mul_f32_e32 v6, v22, v6
	v_mul_f32_e32 v7, v23, v7
	global_store_dword v[46:47], v9, off offset:16
	global_store_dword v[46:47], v10, off offset:24
	global_store_dword v[46:47], v11, off offset:32
	global_store_dword v[46:47], v12, off offset:40
	v_med3_f32 v6, v6, s42, v216
	v_med3_f32 v7, v7, s42, v216
	s_nop 0
	v_cvt_pk_fp8_f32 v9, v6, v7
	v_mul_f32_e32 v8, v38, v48
	v_mul_f32_e32 v6, v39, v48
	v_mul_f32_e32 v8, v24, v8
	v_mul_f32_e32 v6, v25, v6
	v_med3_f32 v8, v8, s42, v216
	v_med3_f32 v6, v6, s42, v216
	v_cvt_pk_fp8_f32 v9, v8, v6 op_sel:[0,0,1]
	v_mul_f32_e32 v6, v40, v48
	v_mul_f32_e32 v2, v2, v6
	v_mul_f32_e32 v6, v41, v48
	v_mul_f32_e32 v3, v3, v6
	v_mul_f32_e32 v6, v42, v48
	v_med3_f32 v2, v2, s42, v216
	v_med3_f32 v3, v3, s42, v216
	v_mul_f32_e32 v4, v4, v6
	s_nop 0
	v_cvt_pk_fp8_f32 v6, v2, v3
	v_mul_f32_e32 v2, v43, v48
	v_mul_f32_e32 v2, v5, v2
	v_med3_f32 v4, v4, s42, v216
	v_med3_f32 v2, v2, s42, v216
	v_cvt_pk_fp8_f32 v6, v4, v2 op_sel:[0,0,1]
	global_store_dword v[46:47], v9, off offset:48
	global_store_dword v[46:47], v6, off offset:56
	s_cbranch_scc0 .LBB0_1885
